# speedup vs baseline: 1.0179x; 1.0179x over previous
_Z11attn_kernelPKDF16_S0_PDF16_:
	s_load_dwordx4 s[4:7], s[0:1], 0x0
	s_load_dwordx2 s[8:9], s[0:1], 0x10
	s_lshr_b32 s1, s2, 3
	s_lshr_b32 s10, s2, 7
	s_and_b32 s0, s2, 4
	s_and_b32 s1, s1, 8
	s_and_b32 s20, s2, 3
	s_lshl_b32 s30, s10, 4
	s_or_b32 s22, s1, s0
	s_or_b32 s0, s30, s20
	s_or_b32 s14, s0, s22
	s_or_b32 s0, s20, 16
	s_sub_i32 s0, s0, s30
	s_mov_b32 s15, 0
	s_or_b32 s0, s0, s22
	s_bfe_u32 s24, s2, 0x30003
	s_ashr_i32 s1, s0, 31
	s_lshl_b64 s[2:3], s[14:15], 18
	s_waitcnt lgkmcnt(0)
	s_add_u32 s2, s4, s2
	s_addc_u32 s3, s5, s3
	s_lshl_b64 s[0:1], s[0:1], 18
	s_add_u32 s11, s4, s0
	s_addc_u32 s12, s5, s1
	s_add_u32 s13, s6, s0
	v_readfirstlane_b32 s16, v0
	s_addc_u32 s18, s7, s1
	s_lshl_b32 s0, s24, 2
	s_lshr_b32 s1, s16, 7
	s_add_i32 s14, s1, s0
	s_lshr_b32 s23, s16, 6
	s_lshl_b64 s[0:1], s[14:15], 13
	s_add_u32 s0, s2, s0
	v_and_b32_e32 v189, 31, v0
	s_addc_u32 s1, s3, s1
	s_lshl_b32 s21, s23, 5
	v_and_or_b32 v1, s21, 32, v189
	v_lshlrev_b32_e32 v186, 4, v1
	v_mov_b32_e32 v187, 0
	s_lshl_b32 s14, s23, 9
	v_lshl_add_u64 v[2:3], s[0:1], 0, v[186:187]
	s_and_b32 s0, s16, 0x3fffffc0
	s_lshl_b64 s[16:17], s[14:15], 1
	v_and_b32_e32 v188, 63, v0
	s_add_u32 s2, s11, s16
	s_addc_u32 s3, s12, s17
	v_lshlrev_b32_e32 v186, 4, v188
	v_lshl_add_u64 v[44:45], s[2:3], 0, v[186:187]
	s_add_u32 s2, s13, s16
	s_addc_u32 s3, s18, s17
	s_lshl_b32 s25, s23, 10
	s_cmp_lg_u32 0, -1
	s_cselect_b32 s1, 0, 0
	v_bfe_u32 v46, v0, 5, 1
	s_add_i32 s25, s25, s1
	s_mov_b32 s1, m0
	s_mov_b32 m0, s25
	s_nop 0
	global_load_lds_dwordx4 v[44:45], off
	s_mov_b32 m0, s1
	v_lshl_add_u64 v[34:35], s[2:3], 0, v[186:187]
	s_add_i32 s26, s25, 0x6000
	v_lshlrev_b32_e32 v4, 10, v46
	s_mov_b32 s1, m0
	s_mov_b32 m0, s26
	s_nop 0
	global_load_lds_dwordx4 v[34:35], off
	s_mov_b32 m0, s1
	s_mov_b64 s[18:19], 0x2000
	v_mov_b32_e32 v5, v187
	v_lshl_add_u64 v[6:7], v[44:45], 0, s[18:19]
	s_add_i32 s1, s25, 0x2000
	s_mov_b32 s2, m0
	s_mov_b32 m0, s1
	s_nop 0
	global_load_lds_dwordx4 v[6:7], off
	s_mov_b32 m0, s2
	v_lshl_add_u64 v[2:3], v[2:3], 0, v[4:5]
	global_load_dwordx4 v[136:139], v[2:3], off
	global_load_dwordx4 v[128:131], v[2:3], off offset:2048
	s_movk_i32 s1, 0x1000
	v_add_co_u32_e32 v2, vcc, s1, v2
	v_lshlrev_b32_e32 v1, 4, v189
	s_nop 0
	v_addc_co_u32_e32 v3, vcc, 0, v3, vcc
	global_load_dwordx4 v[120:123], v[2:3], off
	global_load_dwordx4 v[112:115], v[2:3], off offset:2048
	v_add3_u32 v195, 0, v4, v1
	v_mov_b32_e32 v2, v187
	v_mov_b32_e32 v3, v187
	v_mov_b32_e32 v4, v187
	v_mov_b32_e32 v6, v187
	v_mov_b32_e32 v7, v187
	v_mov_b32_e32 v8, v187
	v_mov_b32_e32 v9, v187
	v_mov_b32_e32 v10, v187
	v_mov_b32_e32 v11, v187
	v_mov_b32_e32 v12, v187
	v_mov_b32_e32 v13, v187
	v_mov_b32_e32 v14, v187
	v_mov_b32_e32 v15, v187
	v_mov_b32_e32 v16, v187
	v_mov_b32_e32 v17, v187
	s_mov_b64 s[2:3], 0x4000
	v_lshl_add_u64 v[18:19], v[44:45], 0, s[2:3]
	s_add_i32 s1, s25, 0x4000
	s_mov_b32 s11, m0
	s_mov_b32 m0, s1
	s_nop 0
	global_load_lds_dwordx4 v[18:19], off
	s_mov_b32 m0, s11
	v_lshl_add_u64 v[18:19], v[34:35], 0, s[18:19]
	s_add_i32 s1, s25, 0x8000
	s_mov_b32 s11, m0
	s_mov_b32 m0, s1
	s_nop 0
	global_load_lds_dwordx4 v[18:19], off
	s_mov_b32 m0, s11
	s_waitcnt vmcnt(4) lgkmcnt(0)
	s_barrier
	ds_read_b128 v[36:39], v195
	ds_read_b128 v[40:43], v195 offset:512
	v_lshlrev_b32_e32 v190, 3, v0
	s_mov_b64 s[12:13], 0x6000
	s_or_b32 s14, s22, s20
	s_sub_i32 s14, s14, s30
	s_add_i32 s34, s14, 16
	s_lshl_b32 s0, s0, 2
	s_ashr_i32 s35, s34, 31
	s_lshl_b64 s[34:35], s[34:35], 18
	s_mov_b32 s27, -1
	s_waitcnt vmcnt(3) lgkmcnt(1)
	v_mfma_f32_32x32x16_f16 v[18:33], v[36:39], v[136:139], v[2:17]
	s_movk_i32 s28, 0x6000
	s_movk_i32 s31, 0x2000
	s_movk_i32 s29, 0x4000
	v_lshlrev_b32_e32 v191, 9, v46
	v_lshlrev_b32_e32 v193, 4, v46
	v_lshl_add_u64 v[180:181], v[34:35], 0, s[12:13]
	s_waitcnt lgkmcnt(0)
	v_mfma_f32_32x32x16_f16 v[2:17], v[40:43], v[136:139], v[2:17]
	ds_read_b128 v[36:39], v195 offset:2048
	ds_read_b128 v[40:43], v195 offset:2560
	s_waitcnt vmcnt(2) lgkmcnt(1)
	v_mfma_f32_32x32x16_f16 v[18:33], v[36:39], v[128:131], v[18:33]
	s_waitcnt lgkmcnt(0)
	v_mfma_f32_32x32x16_f16 v[2:17], v[40:43], v[128:131], v[2:17]
	ds_read_b128 v[36:39], v195 offset:4096
	ds_read_b128 v[40:43], v195 offset:4608
	s_waitcnt vmcnt(1) lgkmcnt(1)
	v_mfma_f32_32x32x16_f16 v[18:33], v[36:39], v[120:123], v[18:33]
	s_waitcnt lgkmcnt(0)
	v_mfma_f32_32x32x16_f16 v[2:17], v[40:43], v[120:123], v[2:17]
	ds_read_b128 v[36:39], v195 offset:6144
	ds_read_b128 v[40:43], v195 offset:6656
	s_waitcnt vmcnt(0) lgkmcnt(1)
	v_mfma_f32_32x32x16_f16 v[18:33], v[36:39], v[112:115], v[18:33]
	s_waitcnt lgkmcnt(0)
	v_mfma_f32_32x32x16_f16 v[2:17], v[40:43], v[112:115], v[2:17]
	s_nop 11
	v_max_f32_e32 v1, v19, v18
	v_max3_f32 v37, v20, v21, v3
	v_max3_f32 v1, v1, v2, v4
	v_max3_f32 v36, v37, v24, v25
	v_max3_f32 v1, v1, v5, v22
	v_max3_f32 v36, v36, v8, v9
	v_max3_f32 v1, v1, v23, v6
	v_max3_f32 v36, v36, v28, v29
	v_max3_f32 v1, v1, v7, v26
	v_max3_f32 v36, v36, v12, v13
	v_max3_f32 v1, v1, v27, v10
	v_max3_f32 v36, v36, v32, v33
	v_max3_f32 v1, v1, v11, v30
	v_max3_f32 v36, v36, v16, v17
	v_max3_f32 v1, v1, v31, v14
	v_max3_f32 v1, v1, v15, v36
	v_mov_b32_e32 v36, v1
	s_nop 1
	v_permlane32_swap_b32_e32 v1, v36
	v_max_f32_e32 v194, v36, v1
	v_lshlrev_b32_e32 v1, 1, v0
	v_sub_f32_e32 v36, v2, v194
	v_and_b32_e32 v1, 32, v1
	v_and_b32_e32 v2, 24, v190
	v_lshlrev_b32_e32 v0, 4, v0
	v_add3_u32 v1, 0, v1, v2
	v_and_b32_e32 v0, 0xc0, v0
	v_lshlrev_b32_e32 v2, 8, v46
	v_add3_u32 v192, v1, v2, v0
	v_xor_b32_e32 v0, 0x80000000, v194
	v_sub_f32_e32 v37, v3, v194
	v_sub_f32_e32 v38, v4, v194
	v_sub_f32_e32 v39, v5, v194
	v_sub_f32_e32 v40, v6, v194
	v_sub_f32_e32 v41, v7, v194
	v_sub_f32_e32 v42, v8, v194
	v_sub_f32_e32 v43, v9, v194
	v_sub_f32_e32 v47, v10, v194
	v_sub_f32_e32 v57, v11, v194
	v_sub_f32_e32 v58, v12, v194
	v_sub_f32_e32 v59, v13, v194
	v_sub_f32_e32 v60, v14, v194
	v_sub_f32_e32 v61, v15, v194
	v_mov_b32_e32 v1, v0
	v_mov_b32_e32 v2, v0
	v_mov_b32_e32 v3, v0
	v_mov_b32_e32 v4, v0
	v_mov_b32_e32 v5, v0
	v_mov_b32_e32 v6, v0
	v_mov_b32_e32 v7, v0
	v_mov_b32_e32 v8, v0
	v_mov_b32_e32 v9, v0
	v_mov_b32_e32 v10, v0
	v_mov_b32_e32 v11, v0
	v_mov_b32_e32 v12, v0
	v_mov_b32_e32 v13, v0
	v_mov_b32_e32 v14, v0
	v_mov_b32_e32 v15, v0
	s_waitcnt vmcnt(0) lgkmcnt(0)
	s_barrier
	v_sub_f32_e32 v62, v16, v194
	v_sub_f32_e32 v63, v17, v194
	v_lshl_add_u64 v[16:17], v[44:45], 0, s[12:13]
	s_mov_b32 s1, m0
	s_mov_b32 m0, s25
	s_nop 0
	global_load_lds_dwordx4 v[16:17], off
	s_mov_b32 m0, s1
	s_add_i32 s1, s25, 0xa000
	v_lshl_add_u64 v[16:17], v[34:35], 0, s[2:3]
	s_mov_b32 s11, m0
	s_mov_b32 m0, s1
	s_nop 0
	global_load_lds_dwordx4 v[16:17], off
	s_mov_b32 m0, s11
	ds_read_b128 v[172:175], v195 offset:8192
	ds_read_b128 v[168:171], v195 offset:8704
	ds_read_b128 v[164:167], v195 offset:10240
	ds_read_b128 v[160:163], v195 offset:10752
	ds_read_b128 v[156:159], v195 offset:12288
	ds_read_b128 v[152:155], v195 offset:12800
	ds_read_b128 v[148:151], v195 offset:14336
	ds_read_b128 v[144:147], v195 offset:14848
	s_add_i32 s11, s0, 0
	v_sub_f32_e32 v18, v18, v194
	v_sub_f32_e32 v19, v19, v194
	v_sub_f32_e32 v20, v20, v194
	v_sub_f32_e32 v21, v21, v194
	v_sub_f32_e32 v22, v22, v194
	v_sub_f32_e32 v23, v23, v194
	v_sub_f32_e32 v24, v24, v194
	v_sub_f32_e32 v25, v25, v194
	v_sub_f32_e32 v26, v26, v194
	v_sub_f32_e32 v27, v27, v194
	v_sub_f32_e32 v28, v28, v194
	v_sub_f32_e32 v29, v29, v194
	v_sub_f32_e32 v30, v30, v194
	v_sub_f32_e32 v31, v31, v194
	v_sub_f32_e32 v32, v32, v194
	v_sub_f32_e32 v33, v33, v194
	s_add_u32 s14, s16, s34
	v_exp_f32_e32 v64, v18
	v_exp_f32_e32 v65, v19
	v_exp_f32_e32 v48, v36
	v_exp_f32_e32 v49, v37
	v_exp_f32_e32 v66, v20
	v_exp_f32_e32 v50, v38
	v_exp_f32_e32 v67, v21
	v_exp_f32_e32 v51, v39
	v_exp_f32_e32 v68, v22
	v_exp_f32_e32 v52, v40
	v_exp_f32_e32 v69, v23
	v_exp_f32_e32 v53, v41
	v_exp_f32_e32 v70, v24
	v_exp_f32_e32 v54, v42
	v_exp_f32_e32 v71, v25
	v_exp_f32_e32 v55, v43
	v_exp_f32_e32 v72, v26
	v_exp_f32_e32 v56, v47
	v_exp_f32_e32 v73, v27
	v_exp_f32_e32 v57, v57
	v_exp_f32_e32 v74, v28
	v_exp_f32_e32 v58, v58
	v_exp_f32_e32 v75, v29
	v_exp_f32_e32 v59, v59
	v_exp_f32_e32 v76, v30
	v_exp_f32_e32 v60, v60
	v_exp_f32_e32 v77, v31
	v_exp_f32_e32 v61, v61
	v_exp_f32_e32 v78, v32
	v_exp_f32_e32 v62, v62
	v_exp_f32_e32 v79, v33
	v_exp_f32_e32 v63, v63
	s_addc_u32 s16, s17, s35
	s_waitcnt vmcnt(2) lgkmcnt(0)
	s_barrier
	v_or_b32_e32 v16, s14, v186
	v_mov_b32_e32 v17, s16
	v_lshl_add_u64 v[16:17], v[16:17], 0, s[18:19]
	v_cmp_gt_u32_e64 s[0:1], 32, v188
	v_lshl_add_u64 v[182:183], s[4:5], 0, v[16:17]
	v_lshl_add_u64 v[184:185], s[6:7], 0, v[16:17]
	s_mov_b32 s16, 0x41000000
	s_mov_b64 s[4:5], 0x8000
	s_movk_i32 s14, 0x2000
	s_movk_i32 s19, 0x4000
	v_mov_b32_e32 v16, v187
	v_mov_b32_e32 v17, v187
	v_mov_b32_e32 v18, v187
	v_mov_b32_e32 v19, v187
	v_mov_b32_e32 v20, v187
	v_mov_b32_e32 v21, v187
	v_mov_b32_e32 v22, v187
	v_mov_b32_e32 v23, v187
	v_mov_b32_e32 v24, v187
	v_mov_b32_e32 v25, v187
	v_mov_b32_e32 v26, v187
	v_mov_b32_e32 v27, v187
	v_mov_b32_e32 v28, v187
	v_mov_b32_e32 v29, v187
	v_mov_b32_e32 v30, v187
	v_mov_b32_e32 v31, v187
	v_mov_b32_e32 v32, v187
	v_mov_b32_e32 v33, v187
	v_mov_b32_e32 v34, v187
	v_mov_b32_e32 v35, v187
	v_mov_b32_e32 v36, v187
	v_mov_b32_e32 v37, v187
	v_mov_b32_e32 v38, v187
	v_mov_b32_e32 v39, v187
	v_mov_b32_e32 v40, v187
	v_mov_b32_e32 v41, v187
	v_mov_b32_e32 v42, v187
	v_mov_b32_e32 v43, v187
	v_mov_b32_e32 v44, v187
	v_mov_b32_e32 v45, v187
	v_mov_b32_e32 v46, v187
	v_mov_b32_e32 v47, v187
	v_lshl_add_u32 v186, v189, 2, s11
.LBB2_1:
	s_mov_b32 s17, s31
	s_mov_b32 s18, s15
	v_add_u32_e32 v196, s18, v192
	ds_read_b64_tr_b16 v[176:177], v196 offset:24576
	ds_read_b64_tr_b16 v[178:179], v196 offset:25088
	s_waitcnt lgkmcnt(9)
	v_mfma_f32_32x32x16_f16 v[96:111], v[172:175], v[136:139], v[0:15]
	v_add_f32_e32 v80, v64, v65
	v_add_f32_e32 v80, v66, v80
	v_add_f32_e32 v80, v67, v80
	v_add_f32_e32 v80, v68, v80
	v_add_f32_e32 v80, v69, v80
	v_cvt_pk_f16_f32 v140, v64, v65
	v_cvt_pk_f16_f32 v141, v66, v67
	ds_read_b64_tr_b16 v[172:173], v196 offset:28672
	ds_read_b64_tr_b16 v[174:175], v196 offset:29184
	v_add_f32_e32 v64, v70, v80
	s_waitcnt lgkmcnt(10)
	v_mfma_f32_32x32x16_f16 v[80:95], v[168:171], v[136:139], v[0:15]
	v_add_f32_e32 v64, v71, v64
	v_add_f32_e32 v64, v72, v64
	v_add_f32_e32 v64, v73, v64
	v_cvt_pk_f16_f32 v142, v68, v69
	v_cvt_pk_f16_f32 v143, v70, v71
	ds_read_b64_tr_b16 v[68:69], v196 offset:25600
	ds_read_b64_tr_b16 v[70:71], v196 offset:26112
	s_waitcnt lgkmcnt(11)
	v_mfma_f32_32x32x16_f16 v[96:111], v[164:167], v[128:131], v[96:111]
	v_add_f32_e32 v64, v74, v64
	v_add_f32_e32 v64, v75, v64
	v_add_f32_e32 v64, v76, v64
	v_add_f32_e32 v116, v77, v64
	v_cvt_pk_f16_f32 v132, v72, v73
	v_cvt_pk_f16_f32 v133, v74, v75
	ds_read_b64_tr_b16 v[64:65], v196 offset:29696
	ds_read_b64_tr_b16 v[66:67], v196 offset:30208
	s_waitcnt lgkmcnt(12)
	v_mfma_f32_32x32x16_f16 v[80:95], v[160:163], v[128:131], v[80:95]
	v_add_f32_e32 v72, v78, v116
	v_add_f32_e32 v72, v79, v72
	v_add_f32_e32 v72, v48, v72
	v_add_f32_e32 v116, v49, v72
	v_cvt_pk_f16_f32 v134, v76, v77
	v_cvt_pk_f16_f32 v135, v78, v79
	ds_read_b64_tr_b16 v[72:73], v196 offset:26624
	ds_read_b64_tr_b16 v[74:75], v196 offset:27136
	s_waitcnt lgkmcnt(13)
	v_mfma_f32_32x32x16_f16 v[96:111], v[156:159], v[120:123], v[96:111]
	v_add_f32_e32 v76, v50, v116
	v_add_f32_e32 v76, v51, v76
	v_add_f32_e32 v76, v52, v76
	v_add_f32_e32 v76, v53, v76
	v_cvt_pk_f16_f32 v124, v48, v49
	v_cvt_pk_f16_f32 v125, v50, v51
	ds_read_b64_tr_b16 v[48:49], v196 offset:30720
	ds_read_b64_tr_b16 v[50:51], v196 offset:31232
	s_waitcnt lgkmcnt(14)
	v_mfma_f32_32x32x16_f16 v[80:95], v[152:155], v[120:123], v[80:95]
	v_add_f32_e32 v76, v54, v76
	v_add_f32_e32 v76, v55, v76
	v_add_f32_e32 v76, v56, v76
	v_add_f32_e32 v76, v57, v76
	v_cvt_pk_f16_f32 v126, v52, v53
	v_cvt_pk_f16_f32 v127, v54, v55
	ds_read_b64_tr_b16 v[52:53], v196 offset:27648
	ds_read_b64_tr_b16 v[54:55], v196 offset:28160
	s_waitcnt lgkmcnt(14)
	v_mfma_f32_32x32x16_f16 v[96:111], v[148:151], v[112:115], v[96:111]
	v_add_f32_e32 v76, v58, v76
	v_add_f32_e32 v76, v59, v76
	v_add_f32_e32 v76, v60, v76
	v_add_f32_e32 v76, v61, v76
	v_cvt_pk_f16_f32 v116, v56, v57
	v_cvt_pk_f16_f32 v117, v58, v59
	ds_read_b64_tr_b16 v[56:57], v196 offset:31744
	ds_read_b64_tr_b16 v[58:59], v196 offset:32256
	v_mfma_f32_32x32x16_f16 v[80:95], v[144:147], v[112:115], v[80:95]
	v_add_f32_e32 v76, v62, v76
	v_add_f32_e32 v76, v63, v76
	v_cvt_pk_f16_f32 v118, v60, v61
	v_cvt_pk_f16_f32 v119, v62, v63
	v_lshl_add_u64 v[60:61], v[182:183], 0, s[12:13]
	s_add_i32 s6, s14, s25
	s_mov_b32 s7, m0
	s_mov_b32 m0, s6
	s_nop 0
	global_load_lds_dwordx4 v[60:61], off
	s_mov_b32 m0, s7
	v_max_f32_e32 v60, v97, v96
	v_add_f32_e32 v187, v187, v76
	v_max3_f32 v61, v98, v99, v81
	v_max3_f32 v60, v60, v80, v82
	v_max3_f32 v60, v60, v83, v100
	v_max3_f32 v61, v61, v102, v103
	v_max3_f32 v60, v60, v101, v84
	v_max3_f32 v61, v61, v86, v87
	v_max3_f32 v60, v60, v85, v104
	v_max3_f32 v61, v61, v106, v107
	v_max3_f32 v60, v60, v105, v88
	v_max3_f32 v61, v61, v90, v91
	v_max3_f32 v60, v60, v89, v108
	v_max3_f32 v61, v61, v110, v111
	v_max3_f32 v60, v60, v109, v92
	v_max3_f32 v61, v61, v94, v95
	v_max3_f32 v60, v60, v93, v61
	v_mov_b32_e32 v61, v60
	s_nop 1
	v_permlane32_swap_b32_e32 v60, v61
	v_max_f32_e32 v60, v61, v60
	s_add_i32 s6, s28, s26
	s_mov_b32 s7, m0
	s_mov_b32 m0, s6
	s_nop 0
	global_load_lds_dwordx4 v[180:181], off
	s_mov_b32 m0, s7
	v_cmp_lt_f32_e32 vcc, s16, v60
	s_cmp_lg_u64 vcc, 0
	s_cselect_b64 s[6:7], -1, 0
	s_cbranch_vccnz .LBB2_9

.LBB2_4:
	v_add_u32_e32 v196, s17, v192
	ds_read_b64_tr_b16 v[144:145], v196 offset:24576
	ds_read_b64_tr_b16 v[146:147], v196 offset:25088
	s_waitcnt lgkmcnt(9)
	v_mfma_f32_32x32x16_f16 v[64:79], v[60:63], v[136:139], v[0:15]
	v_add_f32_e32 v48, v96, v97
	v_add_f32_e32 v48, v98, v48
	v_add_f32_e32 v48, v99, v48
	v_add_f32_e32 v48, v100, v48
	v_add_f32_e32 v48, v101, v48
	v_cvt_pk_f16_f32 v140, v96, v97
	v_cvt_pk_f16_f32 v141, v98, v99
	ds_read_b64_tr_b16 v[152:153], v196 offset:28672
	ds_read_b64_tr_b16 v[154:155], v196 offset:29184
	v_add_f32_e32 v48, v102, v48
	v_add_f32_e32 v48, v103, v48
	v_add_f32_e32 v48, v104, v48
	v_add_f32_e32 v96, v105, v48
	s_waitcnt lgkmcnt(10)
	v_mfma_f32_32x32x16_f16 v[48:63], v[148:151], v[136:139], v[0:15]
	v_cvt_pk_f16_f32 v142, v100, v101
	v_cvt_pk_f16_f32 v143, v102, v103
	ds_read_b64_tr_b16 v[148:149], v196 offset:25600
	ds_read_b64_tr_b16 v[150:151], v196 offset:26112
	s_waitcnt lgkmcnt(11)
	v_mfma_f32_32x32x16_f16 v[64:79], v[176:179], v[128:131], v[64:79]
	v_add_f32_e32 v96, v106, v96
	v_add_f32_e32 v96, v107, v96
	v_add_f32_e32 v96, v108, v96
	v_add_f32_e32 v96, v109, v96
	v_cvt_pk_f16_f32 v132, v104, v105
	v_cvt_pk_f16_f32 v133, v106, v107
	ds_read_b64_tr_b16 v[100:101], v196 offset:29696
	ds_read_b64_tr_b16 v[102:103], v196 offset:30208
	s_waitcnt lgkmcnt(12)
	v_mfma_f32_32x32x16_f16 v[48:63], v[172:175], v[128:131], v[48:63]
	v_add_f32_e32 v96, v110, v96
	v_add_f32_e32 v96, v111, v96
	v_add_f32_e32 v96, v80, v96
	v_add_f32_e32 v104, v81, v96
	v_cvt_pk_f16_f32 v134, v108, v109
	v_cvt_pk_f16_f32 v135, v110, v111
	ds_read_b64_tr_b16 v[96:97], v196 offset:26624
	ds_read_b64_tr_b16 v[98:99], v196 offset:27136
	s_waitcnt lgkmcnt(13)
	v_mfma_f32_32x32x16_f16 v[64:79], v[168:171], v[120:123], v[64:79]
	v_add_f32_e32 v104, v82, v104
	v_add_f32_e32 v104, v83, v104
	v_add_f32_e32 v104, v84, v104
	v_add_f32_e32 v104, v85, v104
	v_cvt_pk_f16_f32 v124, v80, v81
	v_cvt_pk_f16_f32 v125, v82, v83
	ds_read_b64_tr_b16 v[80:81], v196 offset:30720
	ds_read_b64_tr_b16 v[82:83], v196 offset:31232
	s_waitcnt lgkmcnt(14)
	v_mfma_f32_32x32x16_f16 v[48:63], v[164:167], v[120:123], v[48:63]
	v_add_f32_e32 v104, v86, v104
	v_add_f32_e32 v104, v87, v104
	v_add_f32_e32 v104, v88, v104
	v_add_f32_e32 v104, v89, v104
	v_cvt_pk_f16_f32 v126, v84, v85
	v_cvt_pk_f16_f32 v127, v86, v87
	ds_read_b64_tr_b16 v[84:85], v196 offset:27648
	ds_read_b64_tr_b16 v[86:87], v196 offset:28160
	s_waitcnt lgkmcnt(14)
	v_mfma_f32_32x32x16_f16 v[64:79], v[160:163], v[112:115], v[64:79]
	v_add_f32_e32 v104, v90, v104
	v_add_f32_e32 v104, v91, v104
	v_add_f32_e32 v104, v92, v104
	v_add_f32_e32 v104, v93, v104
	v_cvt_pk_f16_f32 v116, v88, v89
	v_cvt_pk_f16_f32 v117, v90, v91
	ds_read_b64_tr_b16 v[88:89], v196 offset:31744
	ds_read_b64_tr_b16 v[90:91], v196 offset:32256
	v_mfma_f32_32x32x16_f16 v[48:63], v[156:159], v[112:115], v[48:63]
	v_add_f32_e32 v104, v94, v104
	v_add_f32_e32 v104, v95, v104
	v_cvt_pk_f16_f32 v118, v92, v93
	v_cvt_pk_f16_f32 v119, v94, v95
	v_lshl_add_u64 v[92:93], v[182:183], 0, s[4:5]
	s_add_i32 s6, s19, s25
	s_mov_b32 s7, m0
	s_mov_b32 m0, s6
	s_nop 0
	global_load_lds_dwordx4 v[92:93], off
	s_mov_b32 m0, s7
	v_lshl_add_u64 v[92:93], v[184:185], 0, s[12:13]
	s_add_i32 s6, s18, s26
	s_mov_b32 s7, m0
	s_mov_b32 m0, s6
	s_nop 0
	global_load_lds_dwordx4 v[92:93], off
	s_mov_b32 m0, s7
	v_max_f32_e32 v92, v65, v64
	v_max3_f32 v93, v66, v67, v49
	v_max3_f32 v92, v92, v48, v50
	v_max3_f32 v92, v92, v51, v68
	v_max3_f32 v93, v93, v70, v71
	v_max3_f32 v92, v92, v69, v52
	v_max3_f32 v93, v93, v54, v55
	v_max3_f32 v92, v92, v53, v72
	v_max3_f32 v93, v93, v74, v75
	v_max3_f32 v92, v92, v73, v56
	v_max3_f32 v93, v93, v58, v59
	v_max3_f32 v92, v92, v57, v76
	v_max3_f32 v93, v93, v78, v79
	v_max3_f32 v92, v92, v77, v60
	v_max3_f32 v93, v93, v62, v63
	v_max3_f32 v92, v92, v61, v93
	v_mov_b32_e32 v93, v92
	s_nop 1
	v_permlane32_swap_b32_e32 v92, v93
	v_max_f32_e32 v92, v93, v92
	v_cmp_lt_f32_e32 vcc, s16, v92
	s_cmp_lg_u64 vcc, 0
	v_add_f32_e32 v187, v187, v104
	s_cselect_b64 s[6:7], -1, 0
	s_cbranch_vccnz .LBB2_12

.LBB2_15:
	ds_read_b64_tr_b16 v[96:97], v192 offset:40960
	ds_read_b64_tr_b16 v[98:99], v192 offset:41472
	v_add_f32_e32 v80, v64, v65
	v_add_f32_e32 v80, v66, v80
	v_add_f32_e32 v80, v67, v80
	v_add_f32_e32 v80, v68, v80
	v_add_f32_e32 v100, v69, v80
	s_waitcnt lgkmcnt(9)
	v_mfma_f32_32x32x16_f16 v[80:95], v[172:175], v[136:139], v[0:15]
	v_cvt_pk_f16_f32 v140, v64, v65
	v_cvt_pk_f16_f32 v141, v66, v67
	ds_read_b64_tr_b16 v[64:65], v192 offset:45056
	ds_read_b64_tr_b16 v[66:67], v192 offset:45568
	s_waitcnt lgkmcnt(10)
	v_mfma_f32_32x32x16_f16 v[0:15], v[168:171], v[136:139], v[0:15]
	v_add_f32_e32 v100, v70, v100
	v_add_f32_e32 v100, v71, v100
	v_add_f32_e32 v100, v72, v100
	v_add_f32_e32 v100, v73, v100
	v_cvt_pk_f16_f32 v142, v68, v69
	v_cvt_pk_f16_f32 v143, v70, v71
	ds_read_b64_tr_b16 v[68:69], v192 offset:41984
	ds_read_b64_tr_b16 v[70:71], v192 offset:42496
	s_waitcnt lgkmcnt(11)
	v_mfma_f32_32x32x16_f16 v[80:95], v[164:167], v[128:131], v[80:95]
	v_add_f32_e32 v100, v74, v100
	v_add_f32_e32 v100, v75, v100
	v_add_f32_e32 v100, v76, v100
	v_add_f32_e32 v100, v77, v100
	v_cvt_pk_f16_f32 v132, v72, v73
	v_cvt_pk_f16_f32 v133, v74, v75
	ds_read_b64_tr_b16 v[72:73], v192 offset:46080
	ds_read_b64_tr_b16 v[74:75], v192 offset:46592
	s_waitcnt lgkmcnt(12)
	v_mfma_f32_32x32x16_f16 v[0:15], v[160:163], v[128:131], v[0:15]
	v_add_f32_e32 v100, v78, v100
	v_add_f32_e32 v100, v79, v100
	v_add_f32_e32 v100, v48, v100
	v_add_f32_e32 v100, v49, v100
	v_cvt_pk_f16_f32 v134, v76, v77
	v_cvt_pk_f16_f32 v135, v78, v79
	ds_read_b64_tr_b16 v[76:77], v192 offset:43008
	ds_read_b64_tr_b16 v[78:79], v192 offset:43520
	s_waitcnt lgkmcnt(13)
	v_mfma_f32_32x32x16_f16 v[80:95], v[156:159], v[120:123], v[80:95]
	v_add_f32_e32 v100, v50, v100
	v_add_f32_e32 v100, v51, v100
	v_add_f32_e32 v100, v52, v100
	v_add_f32_e32 v104, v53, v100
	v_cvt_pk_f16_f32 v124, v48, v49
	v_cvt_pk_f16_f32 v125, v50, v51
	ds_read_b64_tr_b16 v[100:101], v192 offset:47104
	ds_read_b64_tr_b16 v[102:103], v192 offset:47616
	s_waitcnt lgkmcnt(14)
	v_mfma_f32_32x32x16_f16 v[0:15], v[152:155], v[120:123], v[0:15]
	v_add_f32_e32 v48, v54, v104
	v_add_f32_e32 v48, v55, v48
	v_add_f32_e32 v48, v56, v48
	v_add_f32_e32 v48, v57, v48
	v_cvt_pk_f16_f32 v126, v52, v53
	v_cvt_pk_f16_f32 v127, v54, v55
	ds_read_b64_tr_b16 v[104:105], v192 offset:44032
	ds_read_b64_tr_b16 v[106:107], v192 offset:44544
	s_waitcnt lgkmcnt(14)
	v_mfma_f32_32x32x16_f16 v[80:95], v[148:151], v[112:115], v[80:95]
	v_add_f32_e32 v48, v58, v48
	v_add_f32_e32 v48, v59, v48
	v_add_f32_e32 v48, v60, v48
	v_add_f32_e32 v48, v61, v48
	v_cvt_pk_f16_f32 v116, v56, v57
	v_cvt_pk_f16_f32 v117, v58, v59
	ds_read_b64_tr_b16 v[108:109], v192 offset:48128
	ds_read_b64_tr_b16 v[110:111], v192 offset:48640
	v_mfma_f32_32x32x16_f16 v[0:15], v[144:147], v[112:115], v[0:15]
	v_add_f32_e32 v48, v62, v48
	v_add_f32_e32 v48, v63, v48
	v_cvt_pk_f16_f32 v118, v60, v61
	v_cvt_pk_f16_f32 v119, v62, v63
	s_nop 0
	v_add_f32_e32 v112, v187, v48
	v_max_f32_e32 v48, v81, v80
	s_nop 5
	v_max3_f32 v49, v82, v83, v1
	v_max3_f32 v48, v48, v0, v2
	v_max3_f32 v48, v48, v3, v84
	v_max3_f32 v49, v49, v86, v87
	v_max3_f32 v48, v48, v85, v4
	v_max3_f32 v49, v49, v6, v7
	v_max3_f32 v48, v48, v5, v88
	v_max3_f32 v49, v49, v90, v91
	v_max3_f32 v48, v48, v89, v8
	v_max3_f32 v49, v49, v10, v11
	v_max3_f32 v48, v48, v9, v92
	v_max3_f32 v49, v49, v94, v95
	v_max3_f32 v48, v48, v93, v12
	v_max3_f32 v49, v49, v14, v15
	v_max3_f32 v48, v48, v13, v49
	v_mov_b32_e32 v49, v48
	s_nop 1
	v_permlane32_swap_b32_e32 v48, v49
	v_max_f32_e32 v48, v49, v48
	s_mov_b32 s2, 0x41000000
	v_cmp_lt_f32_e32 vcc, s2, v48
	s_cmp_lg_u64 vcc, 0
	s_cselect_b64 s[2:3], -1, 0
	s_cbranch_vccnz .LBB2_21
